# stack12 + grid-barrier poll loops back off s_sleep 3 between polls (back-off tuning below 4)
# baseline (speedup 1.0000x reference)
.LBB0_101:
	global_load_dword v16, v17, s[6:7] sc1
	global_load_dword v1, v17, s[8:9] sc1
	global_load_dword v2, v17, s[10:11] sc1
	global_load_dword v3, v17, s[12:13] sc1
	global_load_dword v4, v17, s[14:15] sc1
	global_load_dword v5, v17, s[16:17] sc1
	global_load_dword v6, v17, s[18:19] sc1
	global_load_dword v7, v17, s[20:21] sc1
	global_load_dword v8, v17, s[22:23] sc1
	global_load_dword v9, v17, s[24:25] sc1
	global_load_dword v10, v17, s[26:27] sc1
	global_load_dword v11, v17, s[28:29] sc1
	global_load_dword v12, v17, s[30:31] sc1
	global_load_dword v13, v17, s[34:35] sc1
	global_load_dword v14, v17, s[36:37] sc1
	global_load_dword v15, v17, s[38:39] sc1
	s_mov_b64 s[40:41], -1
	s_mov_b64 s[42:43], -1
	s_waitcnt vmcnt(14)
	v_add_u32_e32 v18, v1, v16
	s_waitcnt vmcnt(13)
	v_add_u32_e32 v18, v18, v2
	s_waitcnt vmcnt(12)
	v_add_u32_e32 v18, v18, v3
	s_waitcnt vmcnt(11)
	v_add_u32_e32 v18, v18, v4
	s_waitcnt vmcnt(10)
	v_add_u32_e32 v18, v18, v5
	s_waitcnt vmcnt(9)
	v_add_u32_e32 v18, v18, v6
	s_waitcnt vmcnt(8)
	v_add_u32_e32 v18, v18, v7
	s_waitcnt vmcnt(7)
	v_add_u32_e32 v18, v18, v8
	s_waitcnt vmcnt(6)
	v_add_u32_e32 v18, v18, v9
	s_waitcnt vmcnt(5)
	v_add_u32_e32 v18, v18, v10
	s_waitcnt vmcnt(4)
	v_add_u32_e32 v18, v18, v11
	s_waitcnt vmcnt(3)
	v_add_u32_e32 v18, v18, v12
	s_waitcnt vmcnt(2)
	v_add_u32_e32 v18, v18, v13
	s_waitcnt vmcnt(1)
	v_add_u32_e32 v18, v18, v14
	s_waitcnt vmcnt(0)
	v_add_u32_e32 v18, v18, v15
	v_cmp_eq_u32_e32 vcc, s33, v18
	s_cbranch_vccnz .LBB0_100
	s_and_b32 s40, s47, 0xff
	s_cmp_eq_u32 s40, 0
	s_mov_b64 s[40:41], -1
	s_mov_b64 s[44:45], -1
	s_sleep 3
	s_cbranch_scc0 .LBB0_105
	global_load_dword v18, v17, s[4:5] sc1
	s_waitcnt vmcnt(0)
	v_cmp_eq_u32_e32 vcc, 0, v18
	s_cbranch_vccnz .LBB0_107
	s_mov_b64 s[44:45], 0

.LBB0_119:
	s_and_b32 s20, s24, 0xff
	s_mov_b64 s[18:19], -1
	s_cmp_lg_u32 s20, 0
	s_mov_b64 s[22:23], -1
	s_sleep 3
	s_cbranch_scc1 .LBB0_122
	global_load_dword v3, v1, s[10:11] sc1
	s_waitcnt vmcnt(0)
	v_cmp_eq_u32_e32 vcc, 0, v3
	s_cbranch_vccnz .LBB0_124
	s_mov_b64 s[22:23], 0
	s_mov_b64 s[20:21], -1

.LBB0_136:
	s_and_b32 s18, s24, 0xff
	s_cmp_lg_u32 s18, 0
	s_mov_b64 s[20:21], -1
	s_sleep 3
	s_cbranch_scc1 .LBB0_139
	global_load_dword v2, v1, s[10:11] sc1
	s_waitcnt vmcnt(0)
	v_cmp_eq_u32_e32 vcc, 0, v2
	s_cbranch_vccnz .LBB0_141
	s_mov_b64 s[20:21], 0
	s_mov_b64 s[18:19], -1

.LBB0_533:
	global_load_dword v16, v17, s[6:7] sc1
	global_load_dword v1, v17, s[8:9] sc1
	global_load_dword v2, v17, s[10:11] sc1
	global_load_dword v3, v17, s[12:13] sc1
	global_load_dword v4, v17, s[14:15] sc1
	global_load_dword v5, v17, s[16:17] sc1
	global_load_dword v6, v17, s[18:19] sc1
	global_load_dword v7, v17, s[20:21] sc1
	global_load_dword v8, v17, s[22:23] sc1
	global_load_dword v9, v17, s[24:25] sc1
	global_load_dword v10, v17, s[26:27] sc1
	global_load_dword v11, v17, s[28:29] sc1
	global_load_dword v12, v17, s[30:31] sc1
	global_load_dword v13, v17, s[34:35] sc1
	global_load_dword v14, v17, s[36:37] sc1
	global_load_dword v15, v17, s[38:39] sc1
	s_mov_b64 s[40:41], -1
	s_mov_b64 s[42:43], -1
	s_waitcnt vmcnt(14)
	v_add_u32_e32 v18, v1, v16
	s_waitcnt vmcnt(13)
	v_add_u32_e32 v18, v18, v2
	s_waitcnt vmcnt(12)
	v_add_u32_e32 v18, v18, v3
	s_waitcnt vmcnt(11)
	v_add_u32_e32 v18, v18, v4
	s_waitcnt vmcnt(10)
	v_add_u32_e32 v18, v18, v5
	s_waitcnt vmcnt(9)
	v_add_u32_e32 v18, v18, v6
	s_waitcnt vmcnt(8)
	v_add_u32_e32 v18, v18, v7
	s_waitcnt vmcnt(7)
	v_add_u32_e32 v18, v18, v8
	s_waitcnt vmcnt(6)
	v_add_u32_e32 v18, v18, v9
	s_waitcnt vmcnt(5)
	v_add_u32_e32 v18, v18, v10
	s_waitcnt vmcnt(4)
	v_add_u32_e32 v18, v18, v11
	s_waitcnt vmcnt(3)
	v_add_u32_e32 v18, v18, v12
	s_waitcnt vmcnt(2)
	v_add_u32_e32 v18, v18, v13
	s_waitcnt vmcnt(1)
	v_add_u32_e32 v18, v18, v14
	s_waitcnt vmcnt(0)
	v_add_u32_e32 v18, v18, v15
	v_cmp_eq_u32_e32 vcc, s33, v18
	s_cbranch_vccnz .LBB0_532
	s_and_b32 s40, s46, 0xff
	s_cmp_eq_u32 s40, 0
	s_mov_b64 s[40:41], -1
	s_mov_b64 s[44:45], -1
	s_sleep 3
	s_cbranch_scc0 .LBB0_537
	global_load_dword v18, v17, s[4:5] sc1
	s_waitcnt vmcnt(0)
	v_cmp_eq_u32_e32 vcc, 0, v18
	s_cbranch_vccnz .LBB0_539
	s_mov_b64 s[44:45], 0

.LBB0_1358:
	global_load_dword v16, v17, s[8:9] sc1
	global_load_dword v1, v17, s[10:11] sc1
	global_load_dword v2, v17, s[12:13] sc1
	global_load_dword v3, v17, s[14:15] sc1
	global_load_dword v4, v17, s[16:17] sc1
	global_load_dword v5, v17, s[18:19] sc1
	global_load_dword v6, v17, s[20:21] sc1
	global_load_dword v7, v17, s[22:23] sc1
	global_load_dword v8, v17, s[24:25] sc1
	global_load_dword v9, v17, s[26:27] sc1
	global_load_dword v10, v17, s[28:29] sc1
	global_load_dword v11, v17, s[30:31] sc1
	global_load_dword v12, v17, s[34:35] sc1
	global_load_dword v13, v17, s[36:37] sc1
	global_load_dword v14, v17, s[38:39] sc1
	global_load_dword v15, v17, s[40:41] sc1
	s_mov_b64 s[42:43], -1
	s_mov_b64 s[44:45], -1
	s_waitcnt vmcnt(14)
	v_add_u32_e32 v18, v1, v16
	s_waitcnt vmcnt(13)
	v_add_u32_e32 v18, v18, v2
	s_waitcnt vmcnt(12)
	v_add_u32_e32 v18, v18, v3
	s_waitcnt vmcnt(11)
	v_add_u32_e32 v18, v18, v4
	s_waitcnt vmcnt(10)
	v_add_u32_e32 v18, v18, v5
	s_waitcnt vmcnt(9)
	v_add_u32_e32 v18, v18, v6
	s_waitcnt vmcnt(8)
	v_add_u32_e32 v18, v18, v7
	s_waitcnt vmcnt(7)
	v_add_u32_e32 v18, v18, v8
	s_waitcnt vmcnt(6)
	v_add_u32_e32 v18, v18, v9
	s_waitcnt vmcnt(5)
	v_add_u32_e32 v18, v18, v10
	s_waitcnt vmcnt(4)
	v_add_u32_e32 v18, v18, v11
	s_waitcnt vmcnt(3)
	v_add_u32_e32 v18, v18, v12
	s_waitcnt vmcnt(2)
	v_add_u32_e32 v18, v18, v13
	s_waitcnt vmcnt(1)
	v_add_u32_e32 v18, v18, v14
	s_waitcnt vmcnt(0)
	v_add_u32_e32 v18, v18, v15
	v_cmp_eq_u32_e32 vcc, s33, v18
	s_cbranch_vccnz .LBB0_1357
	s_and_b32 s42, s48, 0xff
	s_cmp_eq_u32 s42, 0
	s_mov_b64 s[42:43], -1
	s_mov_b64 s[46:47], -1
	s_sleep 3
	s_cbranch_scc0 .LBB0_1362
	global_load_dword v18, v17, s[6:7] sc1
	s_waitcnt vmcnt(0)
	v_cmp_eq_u32_e32 vcc, 0, v18
	s_cbranch_vccnz .LBB0_1364
	s_mov_b64 s[46:47], 0

.LBB0_1376:
	s_and_b32 s22, s26, 0xff
	s_mov_b64 s[20:21], -1
	s_cmp_lg_u32 s22, 0
	s_mov_b64 s[24:25], -1
	s_sleep 3
	s_cbranch_scc1 .LBB0_1379
	global_load_dword v3, v1, s[12:13] sc1
	s_waitcnt vmcnt(0)
	v_cmp_eq_u32_e32 vcc, 0, v3
	s_cbranch_vccnz .LBB0_1381
	s_mov_b64 s[24:25], 0
	s_mov_b64 s[22:23], -1

.LBB0_1393:
	s_and_b32 s20, s26, 0xff
	s_cmp_lg_u32 s20, 0
	s_mov_b64 s[22:23], -1
	s_sleep 3
	s_cbranch_scc1 .LBB0_1396
	global_load_dword v2, v1, s[12:13] sc1
	s_waitcnt vmcnt(0)
	v_cmp_eq_u32_e32 vcc, 0, v2
	s_cbranch_vccnz .LBB0_1398
	s_mov_b64 s[22:23], 0
	s_mov_b64 s[20:21], -1

.LBB0_1491:
	global_load_dword v16, v17, s[8:9] sc1
	global_load_dword v1, v17, s[10:11] sc1
	global_load_dword v2, v17, s[12:13] sc1
	global_load_dword v3, v17, s[14:15] sc1
	global_load_dword v4, v17, s[16:17] sc1
	global_load_dword v5, v17, s[18:19] sc1
	global_load_dword v6, v17, s[22:23] sc1
	global_load_dword v7, v17, s[24:25] sc1
	global_load_dword v8, v17, s[26:27] sc1
	global_load_dword v9, v17, s[28:29] sc1
	global_load_dword v10, v17, s[30:31] sc1
	global_load_dword v11, v17, s[34:35] sc1
	global_load_dword v12, v17, s[36:37] sc1
	global_load_dword v13, v17, s[38:39] sc1
	global_load_dword v14, v17, s[40:41] sc1
	global_load_dword v15, v17, s[42:43] sc1
	s_mov_b64 s[44:45], -1
	s_mov_b64 s[46:47], -1
	s_waitcnt vmcnt(14)
	v_add_u32_e32 v18, v1, v16
	s_waitcnt vmcnt(13)
	v_add_u32_e32 v18, v18, v2
	s_waitcnt vmcnt(12)
	v_add_u32_e32 v18, v18, v3
	s_waitcnt vmcnt(11)
	v_add_u32_e32 v18, v18, v4
	s_waitcnt vmcnt(10)
	v_add_u32_e32 v18, v18, v5
	s_waitcnt vmcnt(9)
	v_add_u32_e32 v18, v18, v6
	s_waitcnt vmcnt(8)
	v_add_u32_e32 v18, v18, v7
	s_waitcnt vmcnt(7)
	v_add_u32_e32 v18, v18, v8
	s_waitcnt vmcnt(6)
	v_add_u32_e32 v18, v18, v9
	s_waitcnt vmcnt(5)
	v_add_u32_e32 v18, v18, v10
	s_waitcnt vmcnt(4)
	v_add_u32_e32 v18, v18, v11
	s_waitcnt vmcnt(3)
	v_add_u32_e32 v18, v18, v12
	s_waitcnt vmcnt(2)
	v_add_u32_e32 v18, v18, v13
	s_waitcnt vmcnt(1)
	v_add_u32_e32 v18, v18, v14
	s_waitcnt vmcnt(0)
	v_add_u32_e32 v18, v18, v15
	v_cmp_eq_u32_e32 vcc, s33, v18
	s_cbranch_vccnz .LBB0_1490
	s_and_b32 s44, s50, 0xff
	s_cmp_eq_u32 s44, 0
	s_mov_b64 s[44:45], -1
	s_mov_b64 s[48:49], -1
	s_sleep 3
	s_cbranch_scc0 .LBB0_1495
	global_load_dword v18, v17, s[6:7] sc1
	s_waitcnt vmcnt(0)
	v_cmp_eq_u32_e32 vcc, 0, v18
	s_cbranch_vccnz .LBB0_1497
	s_mov_b64 s[48:49], 0

.LBB0_1509:
	s_and_b32 s24, s28, 0xff
	s_mov_b64 s[22:23], -1
	s_cmp_lg_u32 s24, 0
	s_mov_b64 s[26:27], -1
	s_sleep 3
	s_cbranch_scc1 .LBB0_1512
	global_load_dword v3, v1, s[12:13] sc1
	s_waitcnt vmcnt(0)
	v_cmp_eq_u32_e32 vcc, 0, v3
	s_cbranch_vccnz .LBB0_1514
	s_mov_b64 s[26:27], 0
	s_mov_b64 s[24:25], -1

.LBB0_1526:
	s_and_b32 s22, s28, 0xff
	s_cmp_lg_u32 s22, 0
	s_mov_b64 s[24:25], -1
	s_sleep 3
	s_cbranch_scc1 .LBB0_1529
	global_load_dword v2, v1, s[12:13] sc1
	s_waitcnt vmcnt(0)
	v_cmp_eq_u32_e32 vcc, 0, v2
	s_cbranch_vccnz .LBB0_1531
	s_mov_b64 s[24:25], 0
	s_mov_b64 s[22:23], -1

.LBB0_2204:
	global_load_dword v16, v17, s[6:7] sc1
	global_load_dword v1, v17, s[8:9] sc1
	global_load_dword v2, v17, s[10:11] sc1
	global_load_dword v3, v17, s[12:13] sc1
	global_load_dword v4, v17, s[14:15] sc1
	global_load_dword v5, v17, s[16:17] sc1
	global_load_dword v6, v17, s[18:19] sc1
	global_load_dword v7, v17, s[22:23] sc1
	global_load_dword v8, v17, s[24:25] sc1
	global_load_dword v9, v17, s[26:27] sc1
	global_load_dword v10, v17, s[28:29] sc1
	global_load_dword v11, v17, s[30:31] sc1
	global_load_dword v12, v17, s[34:35] sc1
	global_load_dword v13, v17, s[36:37] sc1
	global_load_dword v14, v17, s[38:39] sc1
	global_load_dword v15, v17, s[40:41] sc1
	s_mov_b64 s[42:43], -1
	s_mov_b64 s[44:45], -1
	s_waitcnt vmcnt(14)
	v_add_u32_e32 v18, v1, v16
	s_waitcnt vmcnt(13)
	v_add_u32_e32 v18, v18, v2
	s_waitcnt vmcnt(12)
	v_add_u32_e32 v18, v18, v3
	s_waitcnt vmcnt(11)
	v_add_u32_e32 v18, v18, v4
	s_waitcnt vmcnt(10)
	v_add_u32_e32 v18, v18, v5
	s_waitcnt vmcnt(9)
	v_add_u32_e32 v18, v18, v6
	s_waitcnt vmcnt(8)
	v_add_u32_e32 v18, v18, v7
	s_waitcnt vmcnt(7)
	v_add_u32_e32 v18, v18, v8
	s_waitcnt vmcnt(6)
	v_add_u32_e32 v18, v18, v9
	s_waitcnt vmcnt(5)
	v_add_u32_e32 v18, v18, v10
	s_waitcnt vmcnt(4)
	v_add_u32_e32 v18, v18, v11
	s_waitcnt vmcnt(3)
	v_add_u32_e32 v18, v18, v12
	s_waitcnt vmcnt(2)
	v_add_u32_e32 v18, v18, v13
	s_waitcnt vmcnt(1)
	v_add_u32_e32 v18, v18, v14
	s_waitcnt vmcnt(0)
	v_add_u32_e32 v18, v18, v15
	v_cmp_eq_u32_e32 vcc, s33, v18
	s_cbranch_vccnz .LBB0_2203
	s_and_b32 s42, s48, 0xff
	s_cmp_eq_u32 s42, 0
	s_mov_b64 s[42:43], -1
	s_mov_b64 s[46:47], -1
	s_sleep 3
	s_cbranch_scc0 .LBB0_2208
	global_load_dword v18, v17, s[4:5] sc1
	s_waitcnt vmcnt(0)
	v_cmp_eq_u32_e32 vcc, 0, v18
	s_cbranch_vccnz .LBB0_2210
	s_mov_b64 s[46:47], 0

.LBB0_2222:
	s_and_b32 s22, s26, 0xff
	s_mov_b64 s[18:19], -1
	s_cmp_lg_u32 s22, 0
	s_mov_b64 s[24:25], -1
	s_sleep 3
	s_cbranch_scc1 .LBB0_2225
	global_load_dword v3, v1, s[10:11] sc1
	s_waitcnt vmcnt(0)
	v_cmp_eq_u32_e32 vcc, 0, v3
	s_cbranch_vccnz .LBB0_2227
	s_mov_b64 s[24:25], 0
	s_mov_b64 s[22:23], -1

.LBB0_2239:
	s_and_b32 s18, s26, 0xff
	s_cmp_lg_u32 s18, 0
	s_mov_b64 s[22:23], -1
	s_sleep 3
	s_cbranch_scc1 .LBB0_2242
	global_load_dword v2, v1, s[10:11] sc1
	s_waitcnt vmcnt(0)
	v_cmp_eq_u32_e32 vcc, 0, v2
	s_cbranch_vccnz .LBB0_2244
	s_mov_b64 s[22:23], 0
	s_mov_b64 s[18:19], -1

.LBB0_2307:
	global_load_dword v16, v17, s[6:7] sc1
	global_load_dword v1, v17, s[8:9] sc1
	global_load_dword v2, v17, s[10:11] sc1
	global_load_dword v3, v17, s[12:13] sc1
	global_load_dword v4, v17, s[16:17] sc1
	global_load_dword v5, v17, s[18:19] sc1
	global_load_dword v6, v17, s[22:23] sc1
	global_load_dword v7, v17, s[24:25] sc1
	global_load_dword v8, v17, s[26:27] sc1
	global_load_dword v9, v17, s[28:29] sc1
	global_load_dword v10, v17, s[30:31] sc1
	global_load_dword v11, v17, s[34:35] sc1
	global_load_dword v12, v17, s[36:37] sc1
	global_load_dword v13, v17, s[38:39] sc1
	global_load_dword v14, v17, s[40:41] sc1
	global_load_dword v15, v17, s[42:43] sc1
	s_mov_b64 s[44:45], -1
	s_mov_b64 s[46:47], -1
	s_waitcnt vmcnt(14)
	v_add_u32_e32 v18, v1, v16
	s_waitcnt vmcnt(13)
	v_add_u32_e32 v18, v18, v2
	s_waitcnt vmcnt(12)
	v_add_u32_e32 v18, v18, v3
	s_waitcnt vmcnt(11)
	v_add_u32_e32 v18, v18, v4
	s_waitcnt vmcnt(10)
	v_add_u32_e32 v18, v18, v5
	s_waitcnt vmcnt(9)
	v_add_u32_e32 v18, v18, v6
	s_waitcnt vmcnt(8)
	v_add_u32_e32 v18, v18, v7
	s_waitcnt vmcnt(7)
	v_add_u32_e32 v18, v18, v8
	s_waitcnt vmcnt(6)
	v_add_u32_e32 v18, v18, v9
	s_waitcnt vmcnt(5)
	v_add_u32_e32 v18, v18, v10
	s_waitcnt vmcnt(4)
	v_add_u32_e32 v18, v18, v11
	s_waitcnt vmcnt(3)
	v_add_u32_e32 v18, v18, v12
	s_waitcnt vmcnt(2)
	v_add_u32_e32 v18, v18, v13
	s_waitcnt vmcnt(1)
	v_add_u32_e32 v18, v18, v14
	s_waitcnt vmcnt(0)
	v_add_u32_e32 v18, v18, v15
	v_cmp_eq_u32_e32 vcc, s51, v18
	s_cbranch_vccnz .LBB0_2306
	s_and_b32 s44, s58, 0xff
	s_cmp_eq_u32 s44, 0
	s_mov_b64 s[44:45], -1
	s_mov_b64 s[48:49], -1
	s_sleep 3
	s_cbranch_scc0 .LBB0_2311
	global_load_dword v18, v17, s[4:5] sc1
	s_waitcnt vmcnt(0)
	v_cmp_eq_u32_e32 vcc, 0, v18
	s_cbranch_vccnz .LBB0_2313
	s_mov_b64 s[48:49], 0

.LBB0_2325:
	s_and_b32 s24, s28, 0xff
	s_mov_b64 s[22:23], -1
	s_cmp_lg_u32 s24, 0
	s_mov_b64 s[26:27], -1
	s_sleep 3
	s_cbranch_scc1 .LBB0_2328
	global_load_dword v3, v1, s[10:11] sc1
	s_waitcnt vmcnt(0)
	v_cmp_eq_u32_e32 vcc, 0, v3
	s_cbranch_vccnz .LBB0_2330
	s_mov_b64 s[26:27], 0
	s_mov_b64 s[24:25], -1

.LBB0_2342:
	s_and_b32 s22, s28, 0xff
	s_cmp_lg_u32 s22, 0
	s_mov_b64 s[24:25], -1
	s_sleep 3
	s_cbranch_scc1 .LBB0_2345
	global_load_dword v2, v1, s[10:11] sc1
	s_waitcnt vmcnt(0)
	v_cmp_eq_u32_e32 vcc, 0, v2
	s_cbranch_vccnz .LBB0_2347
	s_mov_b64 s[24:25], 0
	s_mov_b64 s[22:23], -1

.LBB0_2378:
	global_load_dword v16, v17, s[8:9] sc1
	global_load_dword v1, v17, s[10:11] sc1
	global_load_dword v2, v17, s[12:13] sc1
	global_load_dword v3, v17, s[16:17] sc1
	global_load_dword v4, v17, s[18:19] sc1
	global_load_dword v5, v17, s[22:23] sc1
	global_load_dword v6, v17, s[24:25] sc1
	global_load_dword v7, v17, s[26:27] sc1
	global_load_dword v8, v17, s[28:29] sc1
	global_load_dword v9, v17, s[30:31] sc1
	global_load_dword v10, v17, s[34:35] sc1
	global_load_dword v11, v17, s[36:37] sc1
	global_load_dword v12, v17, s[38:39] sc1
	global_load_dword v13, v17, s[40:41] sc1
	global_load_dword v14, v17, s[42:43] sc1
	global_load_dword v15, v17, s[44:45] sc1
	s_mov_b64 s[46:47], -1
	s_mov_b64 s[48:49], -1
	s_waitcnt vmcnt(14)
	v_add_u32_e32 v18, v1, v16
	s_waitcnt vmcnt(13)
	v_add_u32_e32 v18, v18, v2
	s_waitcnt vmcnt(12)
	v_add_u32_e32 v18, v18, v3
	s_waitcnt vmcnt(11)
	v_add_u32_e32 v18, v18, v4
	s_waitcnt vmcnt(10)
	v_add_u32_e32 v18, v18, v5
	s_waitcnt vmcnt(9)
	v_add_u32_e32 v18, v18, v6
	s_waitcnt vmcnt(8)
	v_add_u32_e32 v18, v18, v7
	s_waitcnt vmcnt(7)
	v_add_u32_e32 v18, v18, v8
	s_waitcnt vmcnt(6)
	v_add_u32_e32 v18, v18, v9
	s_waitcnt vmcnt(5)
	v_add_u32_e32 v18, v18, v10
	s_waitcnt vmcnt(4)
	v_add_u32_e32 v18, v18, v11
	s_waitcnt vmcnt(3)
	v_add_u32_e32 v18, v18, v12
	s_waitcnt vmcnt(2)
	v_add_u32_e32 v18, v18, v13
	s_waitcnt vmcnt(1)
	v_add_u32_e32 v18, v18, v14
	s_waitcnt vmcnt(0)
	v_add_u32_e32 v18, v18, v15
	v_cmp_eq_u32_e32 vcc, s59, v18
	s_cbranch_vccnz .LBB0_2377
	s_and_b32 s46, s60, 0xff
	s_cmp_eq_u32 s46, 0
	s_mov_b64 s[46:47], -1
	s_mov_b64 s[50:51], -1
	s_sleep 3
	s_cbranch_scc0 .LBB0_2382
	global_load_dword v18, v17, s[6:7] sc1
	s_waitcnt vmcnt(0)
	v_cmp_eq_u32_e32 vcc, 0, v18
	s_cbranch_vccnz .LBB0_2384
	s_mov_b64 s[50:51], 0

.LBB0_2396:
	s_and_b32 s26, s30, 0xff
	s_mov_b64 s[24:25], -1
	s_cmp_lg_u32 s26, 0
	s_mov_b64 s[28:29], -1
	s_sleep 3
	s_cbranch_scc1 .LBB0_2399
	global_load_dword v3, v1, s[12:13] sc1
	s_waitcnt vmcnt(0)
	v_cmp_eq_u32_e32 vcc, 0, v3
	s_cbranch_vccnz .LBB0_2401
	s_mov_b64 s[28:29], 0
	s_mov_b64 s[26:27], -1

.LBB0_2413:
	s_and_b32 s24, s30, 0xff
	s_cmp_lg_u32 s24, 0
	s_mov_b64 s[26:27], -1
	s_sleep 3
	s_cbranch_scc1 .LBB0_2416
	global_load_dword v2, v1, s[12:13] sc1
	s_waitcnt vmcnt(0)
	v_cmp_eq_u32_e32 vcc, 0, v2
	s_cbranch_vccnz .LBB0_2418
	s_mov_b64 s[26:27], 0
	s_mov_b64 s[24:25], -1

.LBB0_2453:
	global_load_dword v15, v16, s[6:7] sc1
	global_load_dword v0, v16, s[8:9] sc1
	global_load_dword v1, v16, s[10:11] sc1
	global_load_dword v2, v16, s[12:13] sc1
	global_load_dword v3, v16, s[16:17] sc1
	global_load_dword v4, v16, s[18:19] sc1
	global_load_dword v5, v16, s[22:23] sc1
	global_load_dword v6, v16, s[24:25] sc1
	global_load_dword v7, v16, s[26:27] sc1
	global_load_dword v8, v16, s[28:29] sc1
	global_load_dword v9, v16, s[30:31] sc1
	global_load_dword v10, v16, s[34:35] sc1
	global_load_dword v11, v16, s[36:37] sc1
	global_load_dword v12, v16, s[38:39] sc1
	global_load_dword v13, v16, s[40:41] sc1
	global_load_dword v14, v16, s[42:43] sc1
	s_mov_b64 s[44:45], -1
	s_mov_b64 s[46:47], -1
	s_waitcnt vmcnt(14)
	v_add_u32_e32 v17, v0, v15
	s_waitcnt vmcnt(13)
	v_add_u32_e32 v17, v17, v1
	s_waitcnt vmcnt(12)
	v_add_u32_e32 v17, v17, v2
	s_waitcnt vmcnt(11)
	v_add_u32_e32 v17, v17, v3
	s_waitcnt vmcnt(10)
	v_add_u32_e32 v17, v17, v4
	s_waitcnt vmcnt(9)
	v_add_u32_e32 v17, v17, v5
	s_waitcnt vmcnt(8)
	v_add_u32_e32 v17, v17, v6
	s_waitcnt vmcnt(7)
	v_add_u32_e32 v17, v17, v7
	s_waitcnt vmcnt(6)
	v_add_u32_e32 v17, v17, v8
	s_waitcnt vmcnt(5)
	v_add_u32_e32 v17, v17, v9
	s_waitcnt vmcnt(4)
	v_add_u32_e32 v17, v17, v10
	s_waitcnt vmcnt(3)
	v_add_u32_e32 v17, v17, v11
	s_waitcnt vmcnt(2)
	v_add_u32_e32 v17, v17, v12
	s_waitcnt vmcnt(1)
	v_add_u32_e32 v17, v17, v13
	s_waitcnt vmcnt(0)
	v_add_u32_e32 v17, v17, v14
	v_cmp_eq_u32_e32 vcc, s33, v17
	s_cbranch_vccnz .LBB0_2452
	s_and_b32 s44, s50, 0xff
	s_cmp_eq_u32 s44, 0
	s_mov_b64 s[44:45], -1
	s_mov_b64 s[48:49], -1
	s_sleep 3
	s_cbranch_scc0 .LBB0_2457
	global_load_dword v17, v16, s[4:5] sc1
	s_waitcnt vmcnt(0)
	v_cmp_eq_u32_e32 vcc, 0, v17
	s_cbranch_vccnz .LBB0_2459
	s_mov_b64 s[48:49], 0

.LBB0_2471:
	s_and_b32 s24, s28, 0xff
	s_mov_b64 s[22:23], -1
	s_cmp_lg_u32 s24, 0
	s_mov_b64 s[26:27], -1
	s_sleep 3
	s_cbranch_scc1 .LBB0_2474
	global_load_dword v2, v0, s[10:11] sc1
	s_waitcnt vmcnt(0)
	v_cmp_eq_u32_e32 vcc, 0, v2
	s_cbranch_vccnz .LBB0_2476
	s_mov_b64 s[26:27], 0
	s_mov_b64 s[24:25], -1

.LBB0_2488:
	s_and_b32 s22, s28, 0xff
	s_cmp_lg_u32 s22, 0
	s_mov_b64 s[24:25], -1
	s_sleep 3
	s_cbranch_scc1 .LBB0_2491
	global_load_dword v1, v0, s[10:11] sc1
	s_waitcnt vmcnt(0)
	v_cmp_eq_u32_e32 vcc, 0, v1
	s_cbranch_vccnz .LBB0_2493
	s_mov_b64 s[24:25], 0
	s_mov_b64 s[22:23], -1
